# conversion pool split 90/10 between the w_in GEMM phase and the router phase (was 94/6), with 184 GEMM workgroups
# speedup vs baseline: 1.0054x; 1.0054x over previous
; DI CvItem cv_decode(const Params& P, int it) { CvItem c; int item;
;     if (it < NE * CV_GU1) { const int e = it / CV_GU1; c.W = P.in[I_WGU] + (size_t)e * D * 4096; c.N = 4096; c.WT = (unsigned char*)(P.ws + WS_WGU) + (size_t)e * 4096 * D; c.kind = 2; item = it % CV_GU1; }
;     else { const int r = it - NE * CV_GU1; const int e = r / CV_DN1; c.W = P.in[I_WDN] + (size_t)e * D * D; c.N = D; c.WT = (unsigned char*)(P.ws + WS_WDN) + (size_t)e * D * D; c.kind = 3; item = r % CV_DN1; }
;     const int nblk = c.N / 32, kb = item / nblk, nb = item % nblk; c.k0 = 128 * kb; c.n0 = 32 * nb; return c; }
; DI void conv_pool(const Params& P, LAS unsigned char* lds, int pool, int blk_lo, int blk_hi) {
;     ...
;     auto claim = [&]() -> int { unsigned v_ = 0u; if (lane == 0) v_ = __hip_atomic_fetch_add(ctr, 1u, __ATOMIC_RELAXED, __HIP_MEMORY_SCOPE_AGENT); return blk_lo + (int)__builtin_amdgcn_readfirstlane(v_); };
;     const int blk = claim(); if (blk >= CV_NBLK) return;
;     int it = blk * CV_BLK, left = CV_BLK;
;     CvItem cur = cv_decode(P, it); f32x4 v[16]; cv_issue(cur, lane, v);
.LBB0_363:
	s_or_b64 exec, exec, s[2:3]
	v_readfirstlane_b32 s13, v0
	s_cmpk_gt_i32 s13, 0x2b33
	s_cbranch_scc1 .LBB0_383
	s_lshl_b32 s38, s13, 3
	s_cmpk_gt_i32 s13, 0x1fff
	s_mov_b32 s11, 3
	s_cbranch_scc0 .LBB0_366
	s_add_i32 s2, s38, 0xffff0000
	s_lshr_b32 s2, s2, 10
	s_mov_b32 s3, 0
	v_readlane_b32 s48, v254, 6
	s_lshl_b64 s[6:7], s[2:3], 22
	s_lshl_b64 s[2:3], s[2:3], 24
	v_readlane_b32 s50, v254, 8
	v_readlane_b32 s51, v254, 9
	s_add_u32 s14, s50, s2
	v_readlane_b32 s40, v254, 2
	s_addc_u32 s15, s51, s3
	v_readlane_b32 s42, v254, 4
	v_readlane_b32 s43, v254, 5
	s_add_u32 s2, s42, s6
	s_addc_u32 s3, s43, s7
	s_add_u32 s6, s2, 0x12400000
	v_readlane_b32 s49, v254, 7
	v_readlane_b32 s52, v254, 10
	v_readlane_b32 s53, v254, 11
	v_readlane_b32 s54, v254, 12
	v_readlane_b32 s55, v254, 13
	v_readlane_b32 s41, v254, 3
	s_addc_u32 s7, s3, 0
	s_and_b32 s10, s38, 0x3f8
	s_movk_i32 s16, 0x800
	s_cbranch_execz .LBB0_367
	s_branch .LBB0_368

; DI void conv_pool(const Params& P, LAS unsigned char* lds, int pool, int blk_lo, int blk_hi) {
;     ...
;     for (;;) { int nx = it + 1; bool more = true;
;     ...
;         const CvItem nxt = cv_decode(P, nx); f32x4 vn[16]; cv_issue(nxt, lane, vn);
.LBB0_376:
	s_or_b64 exec, exec, s[2:3]
	v_readfirstlane_b32 s2, v56
	s_lshl_b32 s22, s2, 3
	s_cmpk_lt_i32 s2, 0x2b34
	s_cselect_b64 s[2:3], -1, 0
	s_and_b64 s[16:17], s[2:3], exec
	s_cselect_b32 s43, 8, s14
	s_cselect_b32 s44, s22, s38
	s_branch .LBB0_379

; DI CvItem cv_decode(const Params& P, int it) { CvItem c; int item;
;     if (it < NE * CV_GU1) { const int e = it / CV_GU1; c.W = P.in[I_WGU] + (size_t)e * D * 4096; c.N = 4096; c.WT = (unsigned char*)(P.ws + WS_WGU) + (size_t)e * 4096 * D; c.kind = 2; item = it % CV_GU1; }
;     else { const int r = it - NE * CV_GU1; const int e = r / CV_DN1; c.W = P.in[I_WDN] + (size_t)e * D * D; c.N = D; c.WT = (unsigned char*)(P.ws + WS_WDN) + (size_t)e * D * D; c.kind = 3; item = r % CV_DN1; }
;     const int nblk = c.N / 32, kb = item / nblk, nb = item % nblk; c.k0 = 128 * kb; c.n0 = 32 * nb; return c; }
; DI void conv_pool(const Params& P, LAS unsigned char* lds, int pool, int blk_lo, int blk_hi) {
;     ...
;     auto claim = [&]() -> int { unsigned v_ = 0u; if (lane == 0) v_ = __hip_atomic_fetch_add(ctr, 1u, __ATOMIC_RELAXED, __HIP_MEMORY_SCOPE_AGENT); return blk_lo + (int)__builtin_amdgcn_readfirstlane(v_); };
;     const int blk = claim(); if (blk >= CV_NBLK) return;
;     int it = blk * CV_BLK, left = CV_BLK;
;     CvItem cur = cv_decode(P, it); f32x4 v[16]; cv_issue(cur, lane, v);
.LBB0_1116:
	s_or_b64 exec, exec, s[2:3]
	v_readfirstlane_b32 s2, v0
	s_cmpk_gt_i32 s2, 0x4cb
	s_cbranch_scc1 .LBB0_1136
	s_add_i32 s13, s2, 0x2b34
	s_lshl_b32 s20, s13, 3
	s_cmpk_gt_i32 s2, 0xf4cb
	s_mov_b32 s11, 3
	s_cbranch_scc0 .LBB0_1119
	s_add_i32 s2, s20, 0xffff0000
	v_readlane_b32 s36, v254, 6
	s_lshr_b32 s2, s2, 10
	s_mov_b32 s3, 0
	v_readlane_b32 s38, v254, 8
	v_readlane_b32 s39, v254, 9
	s_lshl_b64 s[6:7], s[2:3], 22
	s_lshl_b64 s[2:3], s[2:3], 24
	s_mov_b64 s[14:15], s[38:39]
	s_add_u32 s14, s14, s2
	v_readlane_b32 s16, v254, 2
	s_addc_u32 s15, s15, s3
	v_readlane_b32 s18, v254, 4
	v_readlane_b32 s19, v254, 5
	s_add_u32 s2, s18, s6
	s_addc_u32 s3, s19, s7
	s_add_u32 s6, s2, 0x12400000
	v_readlane_b32 s37, v254, 7
	v_readlane_b32 s40, v254, 10
	v_readlane_b32 s41, v254, 11
	v_readlane_b32 s42, v254, 12
	v_readlane_b32 s43, v254, 13
	v_readlane_b32 s17, v254, 3
	s_addc_u32 s7, s3, 0
	s_and_b32 s10, s20, 0x3f8
	s_movk_i32 s16, 0x800
	s_cbranch_execz .LBB0_1120
	s_branch .LBB0_1121

; DI void conv_pool(const Params& P, LAS unsigned char* lds, int pool, int blk_lo, int blk_hi) {
;     ...
;     for (;;) { int nx = it + 1; bool more = true;
;     ...
;         const CvItem nxt = cv_decode(P, nx); f32x4 vn[16]; cv_issue(nxt, lane, vn);
.LBB0_1129:
	s_or_b64 exec, exec, s[2:3]
	v_readfirstlane_b32 s2, v56
	s_lshl_b32 s3, s2, 3
	s_add_i32 s18, s3, 0x159a0
	s_cmpk_lt_i32 s2, 0x4cc
	s_cselect_b64 s[2:3], -1, 0
	s_and_b64 s[16:17], s[2:3], exec
	s_cselect_b32 s28, 8, s14
	s_cselect_b32 s29, s18, s20
	s_branch .LBB0_1132
